# baseline (speedup 1.0000x reference)
_Z11edge_kernelILi36ELb1EEvPKfS1_PKDF16_PKiS5_S1_S1_S1_S1_S1_PDF16_:
	s_load_dwordx8 s[4:11], s[0:1], 0x0
	s_load_dwordx8 s[12:19], s[0:1], 0x20
	s_load_dwordx4 s[20:23], s[0:1], 0x40
	s_load_dwordx2 s[24:25], s[0:1], 0x50
	v_readfirstlane_b32 s3, v0
	v_bfe_u32 v123, v0, 4, 2
	v_and_b32_e32 v124, 15, v0
	v_and_b32_e32 v111, 63, v0
	s_lshr_b32 s3, s3, 6
	s_lshl_b32 s2, s2, 1
	s_add_i32 s2, s2, s3
	v_lshlrev_b32_e32 v120, 8, v123
	v_lshl_or_b32 v120, v124, 4, v120
	v_lshlrev_b32_e32 v111, 4, v111
	v_lshl_or_b32 v121, v124, 2, v123
	v_lshlrev_b32_e32 v121, 2, v121
	v_mul_u32_u24_e32 v125, 0x900, v123
	v_lshl_or_b32 v125, v124, 4, v125
	v_mul_u32_u24_e32 v110, 36, v123
	s_mul_i32 s28, s2, 0x2400
	s_lshl_b32 s29, s2, 14
	s_lshl_b32 s30, s2, 2
	s_lshl_b32 s31, s2, 8
	s_lshl_b32 s33, s3, 10
	s_lshl_b32 s34, s3, 8
	s_addk_i32 s34, 0x4000
	s_waitcnt lgkmcnt(0)
	s_add_u32 s10, s10, s30
	s_addc_u32 s11, s11, 0
	s_add_u32 s12, s12, s30
	s_addc_u32 s13, s13, 0
	s_load_dword s35, s[10:11], 0x0
	s_load_dword s36, s[12:13], 0x0
	s_add_u32 s14, s14, s28
	s_addc_u32 s15, s15, 0
	global_load_dwordx4 v[0:3], v125, s[14:15] nt
	global_load_dwordx4 v[4:7], v125, s[14:15] offset:256 nt
	global_load_dwordx4 v[8:11], v125, s[14:15] offset:512 nt
	global_load_dwordx4 v[12:15], v125, s[14:15] offset:768 nt
	global_load_dwordx4 v[16:19], v125, s[14:15] offset:1024 nt
	global_load_dwordx4 v[20:23], v125, s[14:15] offset:1280 nt
	global_load_dwordx4 v[24:27], v125, s[14:15] offset:1536 nt
	global_load_dwordx4 v[28:31], v125, s[14:15] offset:1792 nt
	global_load_dwordx4 v[32:35], v125, s[14:15] offset:2048 nt
	s_add_u32 s22, s22, s33
	s_addc_u32 s23, s23, 0
	s_mov_b32 m0, s33
	s_add_u32 s18, s18, s29
	s_addc_u32 s19, s19, 0
	global_load_lds_dwordx4 v111, s[22:23]
	global_load_lds_dwordx4 v111, s[22:23] offset:2048
	s_add_u32 m0, m0, 0x1000
	s_add_u32 s22, s22, 0x1000
	s_addc_u32 s23, s23, 0
	global_load_lds_dwordx4 v111, s[22:23]
	global_load_lds_dwordx4 v111, s[22:23] offset:2048
	s_add_u32 m0, m0, 0x1000
	s_add_u32 s22, s22, 0x1000
	s_addc_u32 s23, s23, 0
	global_load_lds_dwordx4 v111, s[22:23]
	global_load_lds_dwordx4 v111, s[22:23] offset:2048
	s_add_u32 m0, m0, 0x1000
	s_add_u32 s22, s22, 0x1000
	s_addc_u32 s23, s23, 0
	global_load_lds_dwordx4 v111, s[22:23]
	global_load_lds_dwordx4 v111, s[22:23] offset:2048
	s_add_u32 s16, s16, s31
	s_addc_u32 s17, s17, 0
	s_add_u32 s20, s20, s31
	s_addc_u32 s21, s21, 0
	s_waitcnt lgkmcnt(0)
	s_lshl_b32 s36, s36, 7
	s_add_u32 s24, s24, s36
	s_addc_u32 s25, s25, 0
	s_lshl_b32 s37, s35, 7
	s_lshl_b32 s38, s35, 4
	s_add_u32 s4, s4, s37
	s_addc_u32 s5, s5, 0
	s_add_u32 s6, s6, s38
	s_addc_u32 s7, s7, 0
	v_mov_b32_e32 v113, 0
	v_mov_b32_e32 v112, v110
	v_lshl_add_u64 v[126:127], s[4:5], 0, v[112:113]
	v_lshl_add_u64 v[126:127], v[126:127], 0, 20
	v_cmp_eq_u32_e32 vcc, 3, v123
	s_nop 1
	v_mov_b32_e32 v114, s6
	v_mov_b32_e32 v115, s7
	v_cndmask_b32_e32 v126, v126, v114, vcc
	v_cndmask_b32_e32 v127, v127, v115, vcc
	global_load_dwordx4 v[100:103], v110, s[4:5] nt
	global_load_dword v104, v110, s[4:5] offset:16 nt
	global_load_dwordx4 v[106:109], v[126:127], off nt
	global_load_dword v118, v121, s[16:17] nt
	global_load_dword v119, v121, s[20:21] nt
	global_load_dwordx4 v[36:39], v120, s[18:19] nt
	global_load_dwordx4 v[40:43], v120, s[18:19] offset:1024 nt
	global_load_dwordx4 v[44:47], v120, s[18:19] offset:2048 nt
	global_load_dwordx4 v[48:51], v120, s[18:19] offset:3072 nt
	s_add_u32 s18, s18, 0x1000
	s_addc_u32 s19, s19, 0
	global_load_dwordx4 v[52:55], v120, s[18:19] nt
	global_load_dwordx4 v[56:59], v120, s[18:19] offset:1024 nt
	global_load_dwordx4 v[60:63], v120, s[18:19] offset:2048 nt
	global_load_dwordx4 v[64:67], v120, s[18:19] offset:3072 nt
	s_add_u32 s18, s18, 0x1000
	s_addc_u32 s19, s19, 0
	global_load_dwordx4 v[68:71], v120, s[18:19] nt
	global_load_dwordx4 v[72:75], v120, s[18:19] offset:1024 nt
	global_load_dwordx4 v[76:79], v120, s[18:19] offset:2048 nt
	global_load_dwordx4 v[80:83], v120, s[18:19] offset:3072 nt
	s_add_u32 s18, s18, 0x1000
	s_addc_u32 s19, s19, 0
	global_load_dwordx4 v[84:87], v120, s[18:19] nt
	global_load_dwordx4 v[88:91], v120, s[18:19] offset:1024 nt
	global_load_dwordx4 v[92:95], v120, s[18:19] offset:2048 nt
	global_load_dwordx4 v[96:99], v120, s[18:19] offset:3072 nt
	v_lshl_add_u32 v122, v123, 2, s34
	v_add_u32_e32 v121, s34, v121
	v_lshlrev_b32_e32 v125, 3, v124
	v_lshl_or_b32 v125, v123, 2, v125
	s_waitcnt vmcnt(18)
	s_barrier
	v_pk_mul_f32 v[110:111], v[100:101], v[0:1] op_sel_hi:[0,1]
	v_pk_mul_f32 v[112:113], v[100:101], v[2:3] op_sel_hi:[0,1]
	v_pk_mul_f32 v[114:115], v[100:101], v[4:5] op_sel:[1,0]
	v_pk_mul_f32 v[116:117], v[100:101], v[6:7] op_sel:[1,0]
	v_pk_fma_f32 v[110:111], v[102:103], v[8:9], v[110:111] op_sel_hi:[0,1,1]
	v_pk_fma_f32 v[112:113], v[102:103], v[10:11], v[112:113] op_sel_hi:[0,1,1]
	v_pk_fma_f32 v[114:115], v[102:103], v[12:13], v[114:115] op_sel:[1,0,0]
	v_pk_fma_f32 v[116:117], v[102:103], v[14:15], v[116:117] op_sel:[1,0,0]
	v_pk_fma_f32 v[110:111], v[104:105], v[16:17], v[110:111] op_sel_hi:[0,1,1]
	v_pk_fma_f32 v[112:113], v[104:105], v[18:19], v[112:113] op_sel_hi:[0,1,1]
	v_pk_fma_f32 v[114:115], v[106:107], v[20:21], v[114:115] op_sel_hi:[0,1,1]
	v_pk_fma_f32 v[116:117], v[106:107], v[22:23], v[116:117] op_sel_hi:[0,1,1]
	v_pk_fma_f32 v[110:111], v[106:107], v[24:25], v[110:111] op_sel:[1,0,0]
	v_pk_fma_f32 v[112:113], v[106:107], v[26:27], v[112:113] op_sel:[1,0,0]
	v_pk_fma_f32 v[114:115], v[108:109], v[28:29], v[114:115] op_sel_hi:[0,1,1]
	v_pk_fma_f32 v[116:117], v[108:109], v[30:31], v[116:117] op_sel_hi:[0,1,1]
	v_pk_fma_f32 v[110:111], v[108:109], v[32:33], v[110:111] op_sel:[1,0,0]
	v_pk_fma_f32 v[112:113], v[108:109], v[34:35], v[112:113] op_sel:[1,0,0]
	v_pk_add_f32 v[110:111], v[110:111], v[114:115]
	v_pk_add_f32 v[112:113], v[112:113], v[116:117]
	s_nop 1
	v_permlane16_swap_b32_e32 v110, v111
	v_permlane16_swap_b32_e32 v112, v113
	v_add_f32_e32 v110, v110, v111
	v_add_f32_e32 v112, v112, v113
	s_nop 1
	v_permlane32_swap_b32_e32 v110, v112
	v_add_f32_e32 v110, v110, v112
	s_waitcnt vmcnt(17)
	v_add_f32_e32 v110, v110, v118
	v_max_f32_e32 v110, 0, v110
	ds_write_b32 v121, v110
	ds_read2_b32 v[0:1], v122 offset0:0 offset1:4
	ds_read2_b32 v[2:3], v122 offset0:8 offset1:12
	ds_read2_b32 v[4:5], v122 offset0:16 offset1:20
	ds_read2_b32 v[6:7], v122 offset0:24 offset1:28
	ds_read2_b32 v[8:9], v122 offset0:32 offset1:36
	ds_read2_b32 v[10:11], v122 offset0:40 offset1:44
	ds_read2_b32 v[12:13], v122 offset0:48 offset1:52
	ds_read2_b32 v[14:15], v122 offset0:56 offset1:60
	ds_read_b128 v[16:19], v120
	ds_read_b128 v[20:23], v120 offset:1024
	ds_read_b128 v[24:27], v120 offset:2048
	ds_read_b128 v[28:31], v120 offset:3072
	ds_read_b128 v[32:35], v120 offset:4096
	s_waitcnt lgkmcnt(5)
	ds_read_b128 v[100:103], v120 offset:5120
	ds_read_b128 v[104:107], v120 offset:6144
	s_waitcnt vmcnt(12)
	v_pk_mul_f32 v[110:111], v[0:1], v[36:37] op_sel_hi:[0,1]
	v_pk_mul_f32 v[112:113], v[0:1], v[38:39] op_sel_hi:[0,1]
	v_pk_mul_f32 v[114:115], v[0:1], v[40:41] op_sel:[1,0]
	v_pk_mul_f32 v[116:117], v[0:1], v[42:43] op_sel:[1,0]
	v_pk_fma_f32 v[110:111], v[2:3], v[44:45], v[110:111] op_sel_hi:[0,1,1]
	v_pk_fma_f32 v[112:113], v[2:3], v[46:47], v[112:113] op_sel_hi:[0,1,1]
	v_pk_fma_f32 v[114:115], v[2:3], v[48:49], v[114:115] op_sel:[1,0,0]
	v_pk_fma_f32 v[116:117], v[2:3], v[50:51], v[116:117] op_sel:[1,0,0]
	ds_read_b128 v[36:39], v120 offset:7168
	ds_read_b128 v[40:43], v120 offset:8192
	ds_read_b128 v[44:47], v120 offset:9216
	ds_read_b128 v[48:51], v120 offset:10240
	s_waitcnt vmcnt(8)
	v_pk_fma_f32 v[110:111], v[4:5], v[52:53], v[110:111] op_sel_hi:[0,1,1]
	v_pk_fma_f32 v[112:113], v[4:5], v[54:55], v[112:113] op_sel_hi:[0,1,1]
	v_pk_fma_f32 v[114:115], v[4:5], v[56:57], v[114:115] op_sel:[1,0,0]
	v_pk_fma_f32 v[116:117], v[4:5], v[58:59], v[116:117] op_sel:[1,0,0]
	v_pk_fma_f32 v[110:111], v[6:7], v[60:61], v[110:111] op_sel_hi:[0,1,1]
	v_pk_fma_f32 v[112:113], v[6:7], v[62:63], v[112:113] op_sel_hi:[0,1,1]
	v_pk_fma_f32 v[114:115], v[6:7], v[64:65], v[114:115] op_sel:[1,0,0]
	v_pk_fma_f32 v[116:117], v[6:7], v[66:67], v[116:117] op_sel:[1,0,0]
	s_waitcnt lgkmcnt(4)
	ds_read_b128 v[52:55], v120 offset:11264
	ds_read_b128 v[56:59], v120 offset:12288
	ds_read_b128 v[60:63], v120 offset:13312
	ds_read_b128 v[64:67], v120 offset:14336
	s_waitcnt vmcnt(4)
	v_pk_fma_f32 v[110:111], v[8:9], v[68:69], v[110:111] op_sel_hi:[0,1,1]
	v_pk_fma_f32 v[112:113], v[8:9], v[70:71], v[112:113] op_sel_hi:[0,1,1]
	v_pk_fma_f32 v[114:115], v[8:9], v[72:73], v[114:115] op_sel:[1,0,0]
	v_pk_fma_f32 v[116:117], v[8:9], v[74:75], v[116:117] op_sel:[1,0,0]
	v_pk_fma_f32 v[110:111], v[10:11], v[76:77], v[110:111] op_sel_hi:[0,1,1]
	v_pk_fma_f32 v[112:113], v[10:11], v[78:79], v[112:113] op_sel_hi:[0,1,1]
	v_pk_fma_f32 v[114:115], v[10:11], v[80:81], v[114:115] op_sel:[1,0,0]
	v_pk_fma_f32 v[116:117], v[10:11], v[82:83], v[116:117] op_sel:[1,0,0]
	ds_read_b128 v[68:71], v120 offset:15360
	s_waitcnt vmcnt(0)
	v_pk_fma_f32 v[110:111], v[12:13], v[84:85], v[110:111] op_sel_hi:[0,1,1]
	v_pk_fma_f32 v[112:113], v[12:13], v[86:87], v[112:113] op_sel_hi:[0,1,1]
	v_pk_fma_f32 v[114:115], v[12:13], v[88:89], v[114:115] op_sel:[1,0,0]
	v_pk_fma_f32 v[116:117], v[12:13], v[90:91], v[116:117] op_sel:[1,0,0]
	v_pk_fma_f32 v[110:111], v[14:15], v[92:93], v[110:111] op_sel_hi:[0,1,1]
	v_pk_fma_f32 v[112:113], v[14:15], v[94:95], v[112:113] op_sel_hi:[0,1,1]
	v_pk_fma_f32 v[114:115], v[14:15], v[96:97], v[114:115] op_sel:[1,0,0]
	v_pk_fma_f32 v[116:117], v[14:15], v[98:99], v[116:117] op_sel:[1,0,0]
	v_pk_add_f32 v[110:111], v[110:111], v[114:115]
	v_pk_add_f32 v[112:113], v[112:113], v[116:117]
	s_nop 1
	v_permlane16_swap_b32_e32 v110, v111
	v_permlane16_swap_b32_e32 v112, v113
	v_add_f32_e32 v110, v110, v111
	v_add_f32_e32 v112, v112, v113
	s_nop 1
	v_permlane32_swap_b32_e32 v110, v112
	v_add_f32_e32 v110, v110, v112
	v_add_f32_e32 v110, v110, v119
	s_waitcnt lgkmcnt(0)
	ds_write_b32 v121, v110
	ds_read2_b32 v[0:1], v122 offset0:0 offset1:4
	ds_read2_b32 v[2:3], v122 offset0:8 offset1:12
	ds_read2_b32 v[4:5], v122 offset0:16 offset1:20
	ds_read2_b32 v[6:7], v122 offset0:24 offset1:28
	ds_read2_b32 v[8:9], v122 offset0:32 offset1:36
	ds_read2_b32 v[10:11], v122 offset0:40 offset1:44
	ds_read2_b32 v[12:13], v122 offset0:48 offset1:52
	ds_read2_b32 v[14:15], v122 offset0:56 offset1:60
	v_cmp_gt_u32_e32 vcc, 2, v123
	s_waitcnt lgkmcnt(0)
	v_pk_mul_f32 v[110:111], v[0:1], v[16:17] op_sel_hi:[0,1]
	v_pk_mul_f32 v[112:113], v[0:1], v[18:19] op_sel_hi:[0,1]
	v_pk_mul_f32 v[114:115], v[0:1], v[20:21] op_sel:[1,0]
	v_pk_mul_f32 v[116:117], v[0:1], v[22:23] op_sel:[1,0]
	v_pk_fma_f32 v[110:111], v[2:3], v[24:25], v[110:111] op_sel_hi:[0,1,1]
	v_pk_fma_f32 v[112:113], v[2:3], v[26:27], v[112:113] op_sel_hi:[0,1,1]
	v_pk_fma_f32 v[114:115], v[2:3], v[28:29], v[114:115] op_sel:[1,0,0]
	v_pk_fma_f32 v[116:117], v[2:3], v[30:31], v[116:117] op_sel:[1,0,0]
	v_pk_fma_f32 v[110:111], v[4:5], v[32:33], v[110:111] op_sel_hi:[0,1,1]
	v_pk_fma_f32 v[112:113], v[4:5], v[34:35], v[112:113] op_sel_hi:[0,1,1]
	v_pk_fma_f32 v[114:115], v[4:5], v[100:101], v[114:115] op_sel:[1,0,0]
	v_pk_fma_f32 v[116:117], v[4:5], v[102:103], v[116:117] op_sel:[1,0,0]
	v_pk_fma_f32 v[110:111], v[6:7], v[104:105], v[110:111] op_sel_hi:[0,1,1]
	v_pk_fma_f32 v[112:113], v[6:7], v[106:107], v[112:113] op_sel_hi:[0,1,1]
	v_pk_fma_f32 v[114:115], v[6:7], v[36:37], v[114:115] op_sel:[1,0,0]
	v_pk_fma_f32 v[116:117], v[6:7], v[38:39], v[116:117] op_sel:[1,0,0]
	v_pk_fma_f32 v[110:111], v[8:9], v[40:41], v[110:111] op_sel_hi:[0,1,1]
	v_pk_fma_f32 v[112:113], v[8:9], v[42:43], v[112:113] op_sel_hi:[0,1,1]
	v_pk_fma_f32 v[114:115], v[8:9], v[44:45], v[114:115] op_sel:[1,0,0]
	v_pk_fma_f32 v[116:117], v[8:9], v[46:47], v[116:117] op_sel:[1,0,0]
	v_pk_fma_f32 v[110:111], v[10:11], v[48:49], v[110:111] op_sel_hi:[0,1,1]
	v_pk_fma_f32 v[112:113], v[10:11], v[50:51], v[112:113] op_sel_hi:[0,1,1]
	v_pk_fma_f32 v[114:115], v[10:11], v[52:53], v[114:115] op_sel:[1,0,0]
	v_pk_fma_f32 v[116:117], v[10:11], v[54:55], v[116:117] op_sel:[1,0,0]
	v_pk_fma_f32 v[110:111], v[12:13], v[56:57], v[110:111] op_sel_hi:[0,1,1]
	v_pk_fma_f32 v[112:113], v[12:13], v[58:59], v[112:113] op_sel_hi:[0,1,1]
	v_pk_fma_f32 v[114:115], v[12:13], v[60:61], v[114:115] op_sel:[1,0,0]
	v_pk_fma_f32 v[116:117], v[12:13], v[62:63], v[116:117] op_sel:[1,0,0]
	v_pk_fma_f32 v[110:111], v[14:15], v[64:65], v[110:111] op_sel_hi:[0,1,1]
	v_pk_fma_f32 v[112:113], v[14:15], v[66:67], v[112:113] op_sel_hi:[0,1,1]
	v_pk_fma_f32 v[114:115], v[14:15], v[68:69], v[114:115] op_sel:[1,0,0]
	v_pk_fma_f32 v[116:117], v[14:15], v[70:71], v[116:117] op_sel:[1,0,0]
	v_pk_add_f32 v[110:111], v[110:111], v[114:115]
	v_pk_add_f32 v[112:113], v[112:113], v[116:117]
	s_nop 1
	v_permlane16_swap_b32_e32 v110, v112
	v_permlane16_swap_b32_e32 v111, v113
	v_add_f32_e32 v110, v110, v112
	v_add_f32_e32 v111, v111, v113
	v_mov_b32_e32 v126, v110
	v_mov_b32_e32 v127, v111
	s_nop 1
	v_permlane32_swap_b32_e32 v110, v126
	v_permlane32_swap_b32_e32 v111, v127
	v_add_f32_e32 v110, v110, v126
	v_add_f32_e32 v111, v111, v127
	v_cvt_pk_f16_f32 v119, v110, v111
	s_and_saveexec_b64 s[4:5], vcc
	global_atomic_pk_add_f16 v125, v119, s[24:25]
	s_endpgm
	.p2align	8

	.amdhsa_kernel _Z11edge_kernelILi36ELb1EEvPKfS1_PKDF16_PKiS5_S1_S1_S1_S1_S1_PDF16_
		.amdhsa_group_segment_fixed_size 16896
		.amdhsa_private_segment_fixed_size 0
		.amdhsa_kernarg_size 88
		.amdhsa_user_sgpr_count 2
		.amdhsa_user_sgpr_dispatch_ptr 0
		.amdhsa_user_sgpr_queue_ptr 0
		.amdhsa_user_sgpr_kernarg_segment_ptr 1
		.amdhsa_user_sgpr_dispatch_id 0
		.amdhsa_user_sgpr_kernarg_preload_length 0
		.amdhsa_user_sgpr_kernarg_preload_offset 0
		.amdhsa_user_sgpr_private_segment_size 0
		.amdhsa_uses_dynamic_stack 0
		.amdhsa_enable_private_segment 0
		.amdhsa_system_sgpr_workgroup_id_x 1
		.amdhsa_system_sgpr_workgroup_id_y 0
		.amdhsa_system_sgpr_workgroup_id_z 0
		.amdhsa_system_sgpr_workgroup_info 0
		.amdhsa_system_vgpr_workitem_id 0
		.amdhsa_next_free_vgpr 128
		.amdhsa_next_free_sgpr 96
		.amdhsa_accum_offset 128
		.amdhsa_reserve_vcc 1
		.amdhsa_float_round_mode_32 0
		.amdhsa_float_round_mode_16_64 0
		.amdhsa_float_denorm_mode_32 3
		.amdhsa_float_denorm_mode_16_64 3
		.amdhsa_dx10_clamp 1
		.amdhsa_ieee_mode 1
		.amdhsa_fp16_overflow 0
		.amdhsa_tg_split 0
		.amdhsa_exception_fp_ieee_invalid_op 0
		.amdhsa_exception_fp_denorm_src 0
		.amdhsa_exception_fp_ieee_div_zero 0
		.amdhsa_exception_fp_ieee_overflow 0
		.amdhsa_exception_fp_ieee_underflow 0
		.amdhsa_exception_fp_ieee_inexact 0
		.amdhsa_exception_int_div_zero 0
	.end_amdhsa_kernel

amdhsa.kernels:
  - .agpr_count:     8
    .args:
      - .actual_access:  read_only
        .address_space:  global
        .offset:         0
        .size:           8
        .value_kind:     global_buffer
      - .actual_access:  read_only
        .address_space:  global
        .offset:         8
        .size:           8
        .value_kind:     global_buffer
      - .actual_access:  read_only
        .address_space:  global
        .offset:         16
        .size:           8
        .value_kind:     global_buffer
      - .actual_access:  read_only
        .address_space:  global
        .offset:         24
        .size:           8
        .value_kind:     global_buffer
      - .actual_access:  write_only
        .address_space:  global
        .offset:         32
        .size:           8
        .value_kind:     global_buffer
      - .actual_access:  write_only
        .address_space:  global
        .offset:         40
        .size:           8
        .value_kind:     global_buffer
    .group_segment_fixed_size: 4224
    .kernarg_segment_align: 8
    .kernarg_segment_size: 48
    .language:       OpenCL C
    .language_version:
      - 2
      - 0
    .max_flat_workgroup_size: 128
    .name:           _Z11init_kernelPKfS0_S0_S0_PDF16_S1_
    .private_segment_fixed_size: 0
    .sgpr_count:     30
    .sgpr_spill_count: 0
    .symbol:         _Z11init_kernelPKfS0_S0_S0_PDF16_S1_.kd
    .uniform_work_group_size: 1
    .uses_dynamic_stack: false
    .vgpr_count:     68
    .vgpr_spill_count: 0
    .wavefront_size: 64
  - .agpr_count:     8
    .args:
      - .actual_access:  read_only
        .address_space:  global
        .offset:         0
        .size:           8
        .value_kind:     global_buffer
      - .actual_access:  read_only
        .address_space:  global
        .offset:         8
        .size:           8
        .value_kind:     global_buffer
      - .actual_access:  read_only
        .address_space:  global
        .offset:         16
        .size:           8
        .value_kind:     global_buffer
      - .actual_access:  read_only
        .address_space:  global
        .offset:         24
        .size:           8
        .value_kind:     global_buffer
      - .actual_access:  read_only
        .address_space:  global
        .offset:         32
        .size:           8
        .value_kind:     global_buffer
      - .actual_access:  read_only
        .address_space:  global
        .offset:         40
        .size:           8
        .value_kind:     global_buffer
      - .actual_access:  write_only
        .address_space:  global
        .offset:         48
        .size:           8
        .value_kind:     global_buffer
    .group_segment_fixed_size: 4352
    .kernarg_segment_align: 8
    .kernarg_segment_size: 56
    .language:       OpenCL C
    .language_version:
      - 2
      - 0
    .max_flat_workgroup_size: 128
    .name:           _Z12final_kernelPKDF16_S0_PKfS2_S2_S2_Pf
    .private_segment_fixed_size: 0
    .sgpr_count:     30
    .sgpr_spill_count: 0
    .symbol:         _Z12final_kernelPKDF16_S0_PKfS2_S2_S2_Pf.kd
    .uniform_work_group_size: 1
    .uses_dynamic_stack: false
    .vgpr_count:     88
    .vgpr_spill_count: 0
    .wavefront_size: 64
  - .agpr_count:     0
    .args:
      - .actual_access:  read_only
        .address_space:  global
        .offset:         0
        .size:           8
        .value_kind:     global_buffer
      - .actual_access:  read_only
        .address_space:  global
        .offset:         8
        .size:           8
        .value_kind:     global_buffer
      - .actual_access:  read_only
        .address_space:  global
        .offset:         16
        .size:           8
        .value_kind:     global_buffer
      - .actual_access:  read_only
        .address_space:  global
        .offset:         24
        .size:           8
        .value_kind:     global_buffer
      - .actual_access:  read_only
        .address_space:  global
        .offset:         32
        .size:           8
        .value_kind:     global_buffer
      - .actual_access:  read_only
        .address_space:  global
        .offset:         40
        .size:           8
        .value_kind:     global_buffer
      - .actual_access:  read_only
        .address_space:  global
        .offset:         48
        .size:           8
        .value_kind:     global_buffer
      - .actual_access:  read_only
        .address_space:  global
        .offset:         56
        .size:           8
        .value_kind:     global_buffer
      - .actual_access:  read_only
        .address_space:  global
        .offset:         64
        .size:           8
        .value_kind:     global_buffer
      - .actual_access:  read_only
        .address_space:  global
        .offset:         72
        .size:           8
        .value_kind:     global_buffer
      - .address_space:  global
        .offset:         80
        .size:           8
        .value_kind:     global_buffer
    .group_segment_fixed_size: 16896
    .kernarg_segment_align: 8
    .kernarg_segment_size: 88
    .language:       OpenCL C
    .language_version:
      - 2
      - 0
    .max_flat_workgroup_size: 128
    .name:           _Z11edge_kernelILi36ELb1EEvPKfS1_PKDF16_PKiS5_S1_S1_S1_S1_S1_PDF16_
    .private_segment_fixed_size: 0
    .sgpr_count:     45
    .sgpr_spill_count: 0
    .symbol:         _Z11edge_kernelILi36ELb1EEvPKfS1_PKDF16_PKiS5_S1_S1_S1_S1_S1_PDF16_.kd
    .uniform_work_group_size: 1
    .uses_dynamic_stack: false
    .vgpr_count:     128
    .vgpr_spill_count: 0
    .wavefront_size: 64
  - .agpr_count:     0
    .args:
      - .actual_access:  read_only
        .address_space:  global
        .offset:         0
        .size:           8
        .value_kind:     global_buffer
      - .actual_access:  read_only
        .address_space:  global
        .offset:         8
        .size:           8
        .value_kind:     global_buffer
      - .actual_access:  read_only
        .address_space:  global
        .offset:         16
        .size:           8
        .value_kind:     global_buffer
      - .actual_access:  read_only
        .address_space:  global
        .offset:         24
        .size:           8
        .value_kind:     global_buffer
      - .actual_access:  read_only
        .address_space:  global
        .offset:         32
        .size:           8
        .value_kind:     global_buffer
      - .actual_access:  read_only
        .address_space:  global
        .offset:         40
        .size:           8
        .value_kind:     global_buffer
      - .actual_access:  read_only
        .address_space:  global
        .offset:         48
        .size:           8
        .value_kind:     global_buffer
      - .actual_access:  read_only
        .address_space:  global
        .offset:         56
        .size:           8
        .value_kind:     global_buffer
      - .actual_access:  read_only
        .address_space:  global
        .offset:         64
        .size:           8
        .value_kind:     global_buffer
      - .actual_access:  read_only
        .address_space:  global
        .offset:         72
        .size:           8
        .value_kind:     global_buffer
      - .address_space:  global
        .offset:         80
        .size:           8
        .value_kind:     global_buffer
    .group_segment_fixed_size: 16896
    .kernarg_segment_align: 8
    .kernarg_segment_size: 88
    .language:       OpenCL C
    .language_version:
      - 2
      - 0
    .max_flat_workgroup_size: 128
    .name:           _Z11edge_kernelILi64ELb0EEvPKfS1_PKDF16_PKiS5_S1_S1_S1_S1_S1_PDF16_
    .private_segment_fixed_size: 0
    .sgpr_count:     44
    .sgpr_spill_count: 0
    .symbol:         _Z11edge_kernelILi64ELb0EEvPKfS1_PKDF16_PKiS5_S1_S1_S1_S1_S1_PDF16_.kd
    .uniform_work_group_size: 1
    .uses_dynamic_stack: false
    .vgpr_count:     168
    .vgpr_spill_count: 0
    .wavefront_size: 64
